# counted LDS waits also in the P.V sections of the two dilated-attention passes (on top of the MLA counted waits + static priority raise)
# speedup vs baseline: 1.0064x; 1.0064x over previous
; #define FA_SBAR() __builtin_amdgcn_sched_barrier(0)
; #define AA_WRITEV(vv_, i0_) do { _Pragma("unroll") for (int i_ = 0; i_ < 8; ++i_) { const int i = (i0_) + i_; *(LAS v4u*)(Vl + vstb + ((i & 1) + 2 * (i >> 2)) * 2048 + ((i >> 1) & 1) * 256) = vv_[i_]; } } while (0)
; __device__ __forceinline__ void partialSM(f32x16& p0, f32x16& p1, float& m_reg, float& mn, float& alpha, const float C, const float thr) {
;     ...
;   const float mnC = -mn * C;
; #pragma unroll
;   for (int r = 0; r < 16; ++r) p0[r] = fmaf(p0[r], C, mnC);
; #pragma unroll
;   for (int r = 0; r < 16; ++r) p1[r] = fmaf(p1[r], C, mnC);
; #pragma unroll
;   for (int r = 0; r < 16; ++r) p0[r] = __builtin_amdgcn_exp2f(p0[r]);
; }
; __device__ __forceinline__ void finishSM(f32x16& p0, f32x16& p1, float alpha, float& l_reg, bf16x8& pa0, bf16x8& pa1, bf16x8& pa2, bf16x8& pa3) {
; #pragma unroll
;   for (int r = 0; r < 16; ++r) p1[r] = __builtin_amdgcn_exp2f(p1[r]);
;   float ps = 0;
; #pragma unroll
;   for (int r = 0; r < 16; ++r) ps += p0[r];
; #pragma unroll
;   for (int r = 0; r < 16; ++r) ps += p1[r];
;   { auto rr = __builtin_amdgcn_permlane32_swap(__float_as_uint(ps), __float_as_uint(ps), false, false);
;     ps = __uint_as_float(rr[0]) + __uint_as_float(rr[1]); }
;   l_reg = l_reg * alpha + ps;
;   FA_PK4(p0, 0, pa0); FA_PK4(p0, 8, pa1); FA_PK4(p1, 0, pa2); FA_PK4(p1, 8, pa3);
; template <int PASS>
; __device__ __forceinline__ void attn_a_pass(LAS unsigned char* lds_all, const bf16* ZA, bf16* Oabc, float* ML, const float* rel_bias, int gw, int ngw, int xcd, int inx, int tid) {
;     ...
;                 AA_WRITEV(vbq, 8);
;                 asm volatile("s_waitcnt lgkmcnt(0)" ::: "memory"); FA_SBAR();
.LBB0_943:
	v_cndmask_b32_e64 v194, v0, v194, s[6:7]
	v_mul_f32_e32 v0, 0xbe0293ee, v194
	v_fmamk_f32 v80, v162, 0x3e0293ee, v0
	v_fmamk_f32 v81, v163, 0x3e0293ee, v0
	v_fmamk_f32 v84, v84, 0x3e0293ee, v0
	v_fmamk_f32 v85, v85, 0x3e0293ee, v0
	v_fmamk_f32 v86, v86, 0x3e0293ee, v0
	v_fmamk_f32 v87, v87, 0x3e0293ee, v0
	v_fmamk_f32 v88, v88, 0x3e0293ee, v0
	v_fmamk_f32 v89, v89, 0x3e0293ee, v0
	v_fmamk_f32 v90, v90, 0x3e0293ee, v0
	v_fmamk_f32 v91, v91, 0x3e0293ee, v0
	v_fmamk_f32 v92, v92, 0x3e0293ee, v0
	v_fmamk_f32 v93, v93, 0x3e0293ee, v0
	v_fmamk_f32 v94, v94, 0x3e0293ee, v0
	v_fmamk_f32 v95, v95, 0x3e0293ee, v0
	v_fmamk_f32 v82, v82, 0x3e0293ee, v0
	v_fmamk_f32 v83, v83, 0x3e0293ee, v0
	v_fmamk_f32 v96, v96, 0x3e0293ee, v0
	v_fmamk_f32 v97, v97, 0x3e0293ee, v0
	v_fmamk_f32 v68, v68, 0x3e0293ee, v0
	v_fmamk_f32 v69, v69, 0x3e0293ee, v0
	v_fmamk_f32 v70, v70, 0x3e0293ee, v0
	v_fmamk_f32 v71, v71, 0x3e0293ee, v0
	v_fmamk_f32 v72, v72, 0x3e0293ee, v0
	v_fmamk_f32 v73, v73, 0x3e0293ee, v0
	v_fmamk_f32 v74, v74, 0x3e0293ee, v0
	v_fmamk_f32 v75, v75, 0x3e0293ee, v0
	v_fmamk_f32 v76, v76, 0x3e0293ee, v0
	v_fmamk_f32 v77, v77, 0x3e0293ee, v0
	v_fmamk_f32 v78, v78, 0x3e0293ee, v0
	v_fmamk_f32 v79, v79, 0x3e0293ee, v0
	v_fmamk_f32 v66, v66, 0x3e0293ee, v0
	v_fmac_f32_e32 v0, 0x3e0293ee, v67
	v_exp_f32_e32 v67, v80
	v_exp_f32_e32 v80, v81
	v_exp_f32_e32 v81, v84
	v_exp_f32_e32 v84, v85
	v_exp_f32_e32 v85, v86
	v_exp_f32_e32 v173, v66
	v_add_f32_e32 v66, 0, v67
	v_exp_f32_e32 v86, v87
	v_add_f32_e32 v66, v80, v66
	v_exp_f32_e32 v87, v88
	v_add_f32_e32 v66, v81, v66
	v_exp_f32_e32 v88, v89
	v_add_f32_e32 v66, v84, v66
	v_exp_f32_e32 v89, v90
	v_add_f32_e32 v66, v85, v66
	v_exp_f32_e32 v90, v91
	v_add_f32_e32 v66, v86, v66
	v_exp_f32_e32 v91, v92
	v_add_f32_e32 v66, v87, v66
	v_exp_f32_e32 v92, v93
	v_add_f32_e32 v66, v88, v66
	v_exp_f32_e32 v93, v94
	v_add_f32_e32 v66, v89, v66
	v_exp_f32_e32 v94, v95
	v_add_f32_e32 v66, v90, v66
	v_exp_f32_e32 v82, v82
	v_add_f32_e32 v66, v91, v66
	v_exp_f32_e32 v83, v83
	v_add_f32_e32 v66, v92, v66
	v_exp_f32_e32 v95, v96
	v_add_f32_e32 v66, v93, v66
	v_exp_f32_e32 v96, v97
	v_add_f32_e32 v66, v94, v66
	v_exp_f32_e32 v97, v68
	v_add_f32_e32 v66, v82, v66
	v_exp_f32_e32 v162, v69
	v_add_f32_e32 v66, v83, v66
	v_exp_f32_e32 v163, v70
	v_add_f32_e32 v66, v95, v66
	v_exp_f32_e32 v164, v71
	v_add_f32_e32 v66, v96, v66
	v_exp_f32_e32 v165, v72
	v_add_f32_e32 v66, v97, v66
	v_exp_f32_e32 v166, v73
	v_add_f32_e32 v66, v162, v66
	v_exp_f32_e32 v167, v74
	v_add_f32_e32 v66, v163, v66
	v_exp_f32_e32 v168, v75
	v_add_f32_e32 v66, v164, v66
	v_exp_f32_e32 v169, v76
	v_add_f32_e32 v66, v165, v66
	v_exp_f32_e32 v170, v77
	v_add_f32_e32 v66, v166, v66
	v_exp_f32_e32 v171, v78
	v_add_f32_e32 v66, v167, v66
	v_exp_f32_e32 v172, v79
	v_add_f32_e32 v66, v168, v66
	v_add_f32_e32 v66, v169, v66
	v_exp_f32_e32 v0, v0
	v_add_f32_e32 v66, v170, v66
	v_add_f32_e32 v66, v171, v66
	v_add_f32_e32 v66, v172, v66
	v_add_f32_e32 v66, v173, v66
	v_add_f32_e32 v195, v0, v66
	v_mov_b32_e32 v213, v195
	s_nop 1
	v_permlane32_swap_b32_e32 v195, v213
	v_cvt_pk_bf16_f32 v66, v67, v80
	v_cvt_pk_bf16_f32 v67, v81, v84
	v_cvt_pk_bf16_f32 v68, v85, v86
	v_cvt_pk_bf16_f32 v69, v87, v88
	v_cvt_pk_bf16_f32 v70, v89, v90
	v_cvt_pk_bf16_f32 v71, v91, v92
	v_cvt_pk_bf16_f32 v72, v93, v94
	v_cvt_pk_bf16_f32 v73, v82, v83
	v_cvt_pk_bf16_f32 v74, v95, v96
	v_cvt_pk_bf16_f32 v75, v97, v162
	v_cvt_pk_bf16_f32 v76, v163, v164
	v_cvt_pk_bf16_f32 v77, v165, v166
	v_cvt_pk_bf16_f32 v78, v167, v168
	v_cvt_pk_bf16_f32 v79, v169, v170
	v_cvt_pk_bf16_f32 v80, v171, v172
	v_cvt_pk_bf16_f32 v81, v173, v0
	s_nop 0
	v_permlane32_swap_b32_e32 v66, v68
	v_permlane32_swap_b32_e32 v67, v69
	v_permlane32_swap_b32_e32 v70, v72
	v_permlane32_swap_b32_e32 v71, v73
	v_permlane32_swap_b32_e32 v74, v76
	v_permlane32_swap_b32_e32 v75, v77
	v_permlane32_swap_b32_e32 v78, v80
	v_permlane32_swap_b32_e32 v79, v81
	s_waitcnt vmcnt(7)
	ds_write_b128 v210, v[130:133] offset:8192
	s_waitcnt vmcnt(6)
	ds_write_b128 v210, v[134:137] offset:10240
	s_waitcnt vmcnt(5)
	ds_write_b128 v210, v[138:141] offset:8448
	s_waitcnt vmcnt(4)
	ds_write_b128 v210, v[142:145] offset:10496
	s_waitcnt vmcnt(3)
	ds_write_b128 v210, v[146:149] offset:12288
	s_waitcnt vmcnt(2)
	ds_write_b128 v210, v[150:153] offset:14336
	s_waitcnt vmcnt(1)
	ds_write_b128 v210, v[154:157] offset:12544
	s_waitcnt vmcnt(0)
	ds_write_b128 v210, v[158:161] offset:14592
	s_waitcnt lgkmcnt(0)
; #define FA_SBAR() __builtin_amdgcn_sched_barrier(0)
; #define AA_LOADKC(tile_) do { _Pragma("unroll") for (int i_ = 0; i_ < 16; ++i_) { int tk = cls + ((base + (tile_) * 64 + 4 * i_ + vkey) << sh); tk = tk < 0 ? 0 : (tk > SEQ - 1 ? SEQ - 1 : tk); \
;                     kc[i_] = *(const v4u*)(Zbc + (unsigned)tk * (NA * 2) + (ZA_K + vch * 8) * 2); } } while (0)
; template <int PASS>
; __device__ __forceinline__ void attn_a_pass(LAS unsigned char* lds_all, const bf16* ZA, bf16* Oabc, float* ML, const float* rel_bias, int gw, int ngw, int xcd, int inx, int tid) {
;     ...
;                 { const int tn = (tile + 1 < ntile) ? tile + 1 : tile; AA_LOADKC(tn); }
;                 FA_SBAR();
;                 pv_d0(o, vb, pa0, pa1, pa2, pa3);
	s_cmpk_eq_i32 s69, 0xfe00
	s_cselect_b64 s[6:7], -1, 0
	s_and_b64 vcc, s[6:7], exec
	s_cselect_b32 s6, 0x80, s82
	v_add_u32_e32 v172, s6, v197
	v_med3_i32 v0, v172, 0, v230
	v_mul_u32_u24_e32 v0, 0x1800, v0
	v_lshl_add_u64 v[82:83], v[192:193], 0, v[0:1]
	v_max_i32_e32 v0, -4, v172
	v_add_u32_e32 v0, 4, v0
	v_min_u32_e32 v0, 0xfff, v0
	v_mul_u32_u24_e32 v0, 0x1800, v0
	v_lshl_add_u64 v[86:87], v[192:193], 0, v[0:1]
	v_max_i32_e32 v0, -8, v172
	v_add_u32_e32 v0, 8, v0
	v_min_u32_e32 v0, 0xfff, v0
	v_mul_u32_u24_e32 v0, 0x1800, v0
	v_lshl_add_u64 v[90:91], v[192:193], 0, v[0:1]
	v_max_i32_e32 v0, -12, v172
	v_add_u32_e32 v0, 12, v0
	v_min_u32_e32 v0, 0xfff, v0
	v_mul_u32_u24_e32 v0, 0x1800, v0
	v_lshl_add_u64 v[94:95], v[192:193], 0, v[0:1]
	v_max_i32_e32 v0, -16, v172
	v_add_u32_e32 v0, 16, v0
	v_min_u32_e32 v0, 0xfff, v0
	v_mul_u32_u24_e32 v0, 0x1800, v0
	v_lshl_add_u64 v[130:131], v[192:193], 0, v[0:1]
	v_max_i32_e32 v0, 0xffffffec, v172
	v_add_u32_e32 v0, 20, v0
	v_min_u32_e32 v0, 0xfff, v0
	v_mul_u32_u24_e32 v0, 0x1800, v0
	v_lshl_add_u64 v[134:135], v[192:193], 0, v[0:1]
	v_max_i32_e32 v0, 0xffffffe8, v172
	v_add_u32_e32 v0, 24, v0
	v_min_u32_e32 v0, 0xfff, v0
	v_mul_u32_u24_e32 v0, 0x1800, v0
	v_lshl_add_u64 v[138:139], v[192:193], 0, v[0:1]
	v_max_i32_e32 v0, 0xffffffe4, v172
	v_add_u32_e32 v0, 28, v0
	v_min_u32_e32 v0, 0xfff, v0
	v_mul_u32_u24_e32 v0, 0x1800, v0
	v_lshl_add_u64 v[142:143], v[192:193], 0, v[0:1]
	v_max_i32_e32 v0, 0xffffffe0, v172
	v_add_u32_e32 v0, 32, v0
	v_min_u32_e32 v0, 0xfff, v0
	v_mul_u32_u24_e32 v0, 0x1800, v0
	v_lshl_add_u64 v[146:147], v[192:193], 0, v[0:1]
	v_max_i32_e32 v0, 0xffffffdc, v172
	v_add_u32_e32 v0, 36, v0
	v_min_u32_e32 v0, 0xfff, v0
	v_mul_u32_u24_e32 v0, 0x1800, v0
	v_lshl_add_u64 v[150:151], v[192:193], 0, v[0:1]
	v_max_i32_e32 v0, 0xffffffd8, v172
	v_add_u32_e32 v0, 40, v0
	v_min_u32_e32 v0, 0xfff, v0
	v_mul_u32_u24_e32 v0, 0x1800, v0
	v_lshl_add_u64 v[154:155], v[192:193], 0, v[0:1]
	v_max_i32_e32 v0, 0xffffffd4, v172
	v_add_u32_e32 v0, 44, v0
	v_min_u32_e32 v0, 0xfff, v0
	v_mul_u32_u24_e32 v0, 0x1800, v0
	v_lshl_add_u64 v[158:159], v[192:193], 0, v[0:1]
	v_max_i32_e32 v0, 0xffffffd0, v172
	v_add_u32_e32 v0, 48, v0
	v_min_u32_e32 v0, 0xfff, v0
	v_mul_u32_u24_e32 v0, 0x1800, v0
	v_lshl_add_u64 v[162:163], v[192:193], 0, v[0:1]
	v_max_i32_e32 v0, 0xffffffcc, v172
	v_add_u32_e32 v0, 52, v0
	v_min_u32_e32 v0, 0xfff, v0
	v_mul_u32_u24_e32 v0, 0x1800, v0
	v_lshl_add_u64 v[166:167], v[192:193], 0, v[0:1]
	v_max_i32_e32 v0, 0xffffffc8, v172
	v_add_u32_e32 v0, 56, v0
	v_min_u32_e32 v0, 0xfff, v0
	v_mul_u32_u24_e32 v0, 0x1800, v0
	v_lshl_add_u64 v[170:171], v[192:193], 0, v[0:1]
	v_max_i32_e32 v0, 0xffffffc4, v172
	v_add_u32_e32 v0, 60, v0
	v_min_u32_e32 v0, 0xfff, v0
	v_mul_u32_u24_e32 v0, 0x1800, v0
	v_lshl_add_u64 v[174:175], v[192:193], 0, v[0:1]
	global_load_dwordx4 v[82:85], v[82:83], off offset:2048
	s_nop 0
	global_load_dwordx4 v[86:89], v[86:87], off offset:2048
	s_nop 0
	global_load_dwordx4 v[90:93], v[90:91], off offset:2048
	s_nop 0
	global_load_dwordx4 v[94:97], v[94:95], off offset:2048
	s_nop 0
	global_load_dwordx4 v[130:133], v[130:131], off offset:2048
	s_nop 0
	global_load_dwordx4 v[134:137], v[134:135], off offset:2048
	s_nop 0
	global_load_dwordx4 v[138:141], v[138:139], off offset:2048
	s_nop 0
	global_load_dwordx4 v[142:145], v[142:143], off offset:2048
	s_nop 0
	global_load_dwordx4 v[146:149], v[146:147], off offset:2048
	s_nop 0
	global_load_dwordx4 v[150:153], v[150:151], off offset:2048
	s_nop 0
	global_load_dwordx4 v[154:157], v[154:155], off offset:2048
	s_nop 0
	global_load_dwordx4 v[158:161], v[158:159], off offset:2048
	s_nop 0
	global_load_dwordx4 v[162:165], v[162:163], off offset:2048
	s_nop 0
	global_load_dwordx4 v[166:169], v[166:167], off offset:2048
	s_nop 0
	global_load_dwordx4 v[170:173], v[170:171], off offset:2048
	s_nop 0
	global_load_dwordx4 v[174:177], v[174:175], off offset:2048
	ds_read_b64_tr_b16 v[214:215], v199 offset:0
	ds_read_b64_tr_b16 v[216:217], v199 offset:0x800
	ds_read_b64_tr_b16 v[236:237], v199 offset:0x1000
	ds_read_b64_tr_b16 v[238:239], v199 offset:0x1800
	ds_read_b64_tr_b16 v[240:241], v199 offset:0x2000
	ds_read_b64_tr_b16 v[242:243], v199 offset:0x2800
	ds_read_b64_tr_b16 v[244:245], v199 offset:0x3000
	ds_read_b64_tr_b16 v[246:247], v199 offset:0x3800
	s_nop 0
	s_waitcnt lgkmcnt(6)
; #define FA_SBAR() __builtin_amdgcn_sched_barrier(0)
; #define AA_WRITEKC() do { _Pragma("unroll") for (int i_ = 0; i_ < 16; ++i_) *(LAS v4u*)(Vl + i_ * 1024 + ((i_ & 1) ? (kst0 ^ 64) : kst0)) = kc[i_]; } while (0)
;   s16x4 l0 = tr_read<BASE + v_rd_off(D0, 0, 0)>(vb), h0 = tr_read<BASE + v_rd_off(D0, 0, 1)>(vb), l1 = tr_read<BASE + v_rd_off(D0, 1, 0)>(vb), h1 = tr_read<BASE + v_rd_off(D0, 1, 1)>(vb);
;   s16x4 l2 = tr_read<BASE + v_rd_off(D0, 2, 0)>(vb), h2 = tr_read<BASE + v_rd_off(D0, 2, 1)>(vb), l3 = tr_read<BASE + v_rd_off(D0, 3, 0)>(vb), h3 = tr_read<BASE + v_rd_off(D0, 3, 1)>(vb);
;   asm volatile("s_waitcnt lgkmcnt(0)" : "+v"(l0), "+v"(h0), "+v"(l1), "+v"(h1), "+v"(l2), "+v"(h2), "+v"(l3), "+v"(h3) :: "memory"); FA_SBAR();
;     ...
;   od = __builtin_amdgcn_mfma_f32_32x32x16_bf16(pa0, FA_PK(l0, h0), od, 0, 0, 0);
;   od = __builtin_amdgcn_mfma_f32_32x32x16_bf16(pa1, FA_PK(l1, h1), od, 0, 0, 0);
;   od = __builtin_amdgcn_mfma_f32_32x32x16_bf16(pa2, FA_PK(l2, h2), od, 0, 0, 0);
;   od = __builtin_amdgcn_mfma_f32_32x32x16_bf16(pa3, FA_PK(l3, h3), od, 0, 0, 0);
;     ...
; }
;   pv_one<0, BASE>(o[0], vb, pa0, pa1, pa2, pa3); pv_one<1, BASE>(o[1], vb, pa0, pa1, pa2, pa3); pv_one<2, BASE>(o[2], vb, pa0, pa1, pa2, pa3); pv_one<3, BASE>(o[3], vb, pa0, pa1, pa2, pa3);
; template <int PASS>
; __device__ __forceinline__ void attn_a_pass(LAS unsigned char* lds_all, const bf16* ZA, bf16* Oabc, float* ML, const float* rel_bias, int gw, int ngw, int xcd, int inx, int tid) {
;     ...
;                 if (tile + 1 < ntile) AA_WRITEKC();
	s_nop 0
	v_mfma_f32_32x32x16_bf16 v[50:65], v[66:69], v[214:217], v[50:65]
	ds_read_b64_tr_b16 v[214:215], v199 offset:0x200
	ds_read_b64_tr_b16 v[216:217], v199 offset:0xa00
	s_waitcnt lgkmcnt(6)
	v_mfma_f32_32x32x16_bf16 v[50:65], v[70:73], v[236:239], v[50:65]
	ds_read_b64_tr_b16 v[236:237], v199 offset:0x1200
	ds_read_b64_tr_b16 v[238:239], v199 offset:0x1a00
	s_waitcnt lgkmcnt(6)
	v_mfma_f32_32x32x16_bf16 v[50:65], v[74:77], v[240:243], v[50:65]
	ds_read_b64_tr_b16 v[240:241], v199 offset:0x2200
	ds_read_b64_tr_b16 v[242:243], v199 offset:0x2a00
	s_waitcnt lgkmcnt(6)
	v_mfma_f32_32x32x16_bf16 v[50:65], v[78:81], v[244:247], v[50:65]
	ds_read_b64_tr_b16 v[244:245], v199 offset:0x3200
	ds_read_b64_tr_b16 v[246:247], v199 offset:0x3a00
	s_nop 0
	s_waitcnt lgkmcnt(6)
	s_nop 0
	v_mfma_f32_32x32x16_bf16 v[34:49], v[66:69], v[214:217], v[34:49]
	ds_read_b64_tr_b16 v[214:215], v199 offset:0x400
	ds_read_b64_tr_b16 v[216:217], v199 offset:0xc00
	s_waitcnt lgkmcnt(6)
	v_mfma_f32_32x32x16_bf16 v[34:49], v[70:73], v[236:239], v[34:49]
	ds_read_b64_tr_b16 v[236:237], v199 offset:0x1400
	ds_read_b64_tr_b16 v[238:239], v199 offset:0x1c00
	s_waitcnt lgkmcnt(6)
	v_mfma_f32_32x32x16_bf16 v[34:49], v[74:77], v[240:243], v[34:49]
	ds_read_b64_tr_b16 v[240:241], v199 offset:0x2400
	ds_read_b64_tr_b16 v[242:243], v199 offset:0x2c00
	s_waitcnt lgkmcnt(6)
	v_mfma_f32_32x32x16_bf16 v[34:49], v[78:81], v[244:247], v[34:49]
	ds_read_b64_tr_b16 v[244:245], v199 offset:0x3400
	ds_read_b64_tr_b16 v[246:247], v199 offset:0x3c00
	s_nop 0
	s_waitcnt lgkmcnt(6)
	s_nop 0
	v_mfma_f32_32x32x16_bf16 v[18:33], v[66:69], v[214:217], v[18:33]
	ds_read_b64_tr_b16 v[214:215], v199 offset:0x600
	ds_read_b64_tr_b16 v[216:217], v199 offset:0xe00
	s_waitcnt lgkmcnt(6)
	v_mfma_f32_32x32x16_bf16 v[18:33], v[70:73], v[236:239], v[18:33]
	ds_read_b64_tr_b16 v[236:237], v199 offset:0x1600
	ds_read_b64_tr_b16 v[238:239], v199 offset:0x1e00
	s_waitcnt lgkmcnt(6)
	v_mfma_f32_32x32x16_bf16 v[18:33], v[74:77], v[240:243], v[18:33]
	ds_read_b64_tr_b16 v[240:241], v199 offset:0x2600
	ds_read_b64_tr_b16 v[242:243], v199 offset:0x2e00
	s_waitcnt lgkmcnt(6)
	v_mfma_f32_32x32x16_bf16 v[18:33], v[78:81], v[244:247], v[18:33]
	ds_read_b64_tr_b16 v[244:245], v199 offset:0x3600
	ds_read_b64_tr_b16 v[246:247], v199 offset:0x3e00
	s_nop 0
	s_waitcnt lgkmcnt(6)
	s_nop 0
	v_mfma_f32_32x32x16_bf16 v[2:17], v[66:69], v[214:217], v[2:17]
	s_waitcnt lgkmcnt(4)
	v_mfma_f32_32x32x16_bf16 v[2:17], v[70:73], v[236:239], v[2:17]
	s_waitcnt lgkmcnt(2)
	v_mfma_f32_32x32x16_bf16 v[2:17], v[74:77], v[240:243], v[2:17]
	s_waitcnt lgkmcnt(0)
	v_mfma_f32_32x32x16_bf16 v[2:17], v[78:81], v[244:247], v[2:17]
	s_cbranch_vccnz .LBB0_945
	s_waitcnt vmcnt(15)
	ds_write_b128 v200, v[82:85]
	s_waitcnt vmcnt(14)
	ds_write_b128 v201, v[86:89] offset:1024
	s_waitcnt vmcnt(13)
	ds_write_b128 v200, v[90:93] offset:2048
	s_waitcnt vmcnt(12)
	ds_write_b128 v201, v[94:97] offset:3072
	s_waitcnt vmcnt(11)
	ds_write_b128 v200, v[130:133] offset:4096
	s_waitcnt vmcnt(10)
	ds_write_b128 v201, v[134:137] offset:5120
	s_waitcnt vmcnt(9)
	ds_write_b128 v200, v[138:141] offset:6144
	s_waitcnt vmcnt(8)
	ds_write_b128 v201, v[142:145] offset:7168
	s_waitcnt vmcnt(7)
	ds_write_b128 v200, v[146:149] offset:8192
	s_waitcnt vmcnt(6)
	ds_write_b128 v201, v[150:153] offset:9216
	s_waitcnt vmcnt(5)
	ds_write_b128 v200, v[154:157] offset:10240
	s_waitcnt vmcnt(4)
	ds_write_b128 v201, v[158:161] offset:11264
	s_waitcnt vmcnt(3)
	ds_write_b128 v200, v[162:165] offset:12288
	s_waitcnt vmcnt(2)
	ds_write_b128 v201, v[166:169] offset:13312
	s_waitcnt vmcnt(1)
	ds_write_b128 v200, v[170:173] offset:14336
	s_waitcnt vmcnt(0)
	ds_write_b128 v201, v[174:177] offset:15360

; #define FA_SBAR() __builtin_amdgcn_sched_barrier(0)
; #define AA_WRITEV(vv_, i0_) do { _Pragma("unroll") for (int i_ = 0; i_ < 8; ++i_) { const int i = (i0_) + i_; *(LAS v4u*)(Vl + vstb + ((i & 1) + 2 * (i >> 2)) * 2048 + ((i >> 1) & 1) * 256) = vv_[i_]; } } while (0)
; __device__ __forceinline__ void partialSM(f32x16& p0, f32x16& p1, float& m_reg, float& mn, float& alpha, const float C, const float thr) {
;     ...
;   const float mnC = -mn * C;
; #pragma unroll
;   for (int r = 0; r < 16; ++r) p0[r] = fmaf(p0[r], C, mnC);
; #pragma unroll
;   for (int r = 0; r < 16; ++r) p1[r] = fmaf(p1[r], C, mnC);
; #pragma unroll
;   for (int r = 0; r < 16; ++r) p0[r] = __builtin_amdgcn_exp2f(p0[r]);
; }
; __device__ __forceinline__ void finishSM(f32x16& p0, f32x16& p1, float alpha, float& l_reg, bf16x8& pa0, bf16x8& pa1, bf16x8& pa2, bf16x8& pa3) {
; #pragma unroll
;   for (int r = 0; r < 16; ++r) p1[r] = __builtin_amdgcn_exp2f(p1[r]);
;   float ps = 0;
; #pragma unroll
;   for (int r = 0; r < 16; ++r) ps += p0[r];
; #pragma unroll
;   for (int r = 0; r < 16; ++r) ps += p1[r];
;   { auto rr = __builtin_amdgcn_permlane32_swap(__float_as_uint(ps), __float_as_uint(ps), false, false);
;     ps = __uint_as_float(rr[0]) + __uint_as_float(rr[1]); }
;   l_reg = l_reg * alpha + ps;
;   FA_PK4(p0, 0, pa0); FA_PK4(p0, 8, pa1); FA_PK4(p1, 0, pa2); FA_PK4(p1, 8, pa3);
; template <int PASS>
; __device__ __forceinline__ void attn_a_pass(LAS unsigned char* lds_all, const bf16* ZA, bf16* Oabc, float* ML, const float* rel_bias, int gw, int ngw, int xcd, int inx, int tid) {
;     ...
;                 AA_WRITEV(vbq, 8);
;                 asm volatile("s_waitcnt lgkmcnt(0)" ::: "memory"); FA_SBAR();
.LBB0_1028:
	v_cndmask_b32_e64 v190, v0, v190, s[6:7]
	v_mul_f32_e32 v0, 0xbe0293ee, v190
	v_fmamk_f32 v80, v162, 0x3e0293ee, v0
	v_fmamk_f32 v81, v163, 0x3e0293ee, v0
	v_fmamk_f32 v84, v84, 0x3e0293ee, v0
	v_fmamk_f32 v85, v85, 0x3e0293ee, v0
	v_fmamk_f32 v86, v86, 0x3e0293ee, v0
	v_fmamk_f32 v87, v87, 0x3e0293ee, v0
	v_fmamk_f32 v88, v88, 0x3e0293ee, v0
	v_fmamk_f32 v89, v89, 0x3e0293ee, v0
	v_fmamk_f32 v90, v90, 0x3e0293ee, v0
	v_fmamk_f32 v91, v91, 0x3e0293ee, v0
	v_fmamk_f32 v92, v92, 0x3e0293ee, v0
	v_fmamk_f32 v93, v93, 0x3e0293ee, v0
	v_fmamk_f32 v94, v94, 0x3e0293ee, v0
	v_fmamk_f32 v95, v95, 0x3e0293ee, v0
	v_fmamk_f32 v82, v82, 0x3e0293ee, v0
	v_fmamk_f32 v83, v83, 0x3e0293ee, v0
	v_fmamk_f32 v96, v96, 0x3e0293ee, v0
	v_fmamk_f32 v97, v97, 0x3e0293ee, v0
	v_fmamk_f32 v68, v68, 0x3e0293ee, v0
	v_fmamk_f32 v69, v69, 0x3e0293ee, v0
	v_fmamk_f32 v70, v70, 0x3e0293ee, v0
	v_fmamk_f32 v71, v71, 0x3e0293ee, v0
	v_fmamk_f32 v72, v72, 0x3e0293ee, v0
	v_fmamk_f32 v73, v73, 0x3e0293ee, v0
	v_fmamk_f32 v74, v74, 0x3e0293ee, v0
	v_fmamk_f32 v75, v75, 0x3e0293ee, v0
	v_fmamk_f32 v76, v76, 0x3e0293ee, v0
	v_fmamk_f32 v77, v77, 0x3e0293ee, v0
	v_fmamk_f32 v78, v78, 0x3e0293ee, v0
	v_fmamk_f32 v79, v79, 0x3e0293ee, v0
	v_fmamk_f32 v66, v66, 0x3e0293ee, v0
	v_fmac_f32_e32 v0, 0x3e0293ee, v67
	v_exp_f32_e32 v67, v80
	v_exp_f32_e32 v80, v81
	v_exp_f32_e32 v81, v84
	v_exp_f32_e32 v84, v85
	v_exp_f32_e32 v85, v86
	v_exp_f32_e32 v173, v66
	v_add_f32_e32 v66, 0, v67
	v_exp_f32_e32 v86, v87
	v_add_f32_e32 v66, v80, v66
	v_exp_f32_e32 v87, v88
	v_add_f32_e32 v66, v81, v66
	v_exp_f32_e32 v88, v89
	v_add_f32_e32 v66, v84, v66
	v_exp_f32_e32 v89, v90
	v_add_f32_e32 v66, v85, v66
	v_exp_f32_e32 v90, v91
	v_add_f32_e32 v66, v86, v66
	v_exp_f32_e32 v91, v92
	v_add_f32_e32 v66, v87, v66
	v_exp_f32_e32 v92, v93
	v_add_f32_e32 v66, v88, v66
	v_exp_f32_e32 v93, v94
	v_add_f32_e32 v66, v89, v66
	v_exp_f32_e32 v94, v95
	v_add_f32_e32 v66, v90, v66
	v_exp_f32_e32 v82, v82
	v_add_f32_e32 v66, v91, v66
	v_exp_f32_e32 v83, v83
	v_add_f32_e32 v66, v92, v66
	v_exp_f32_e32 v95, v96
	v_add_f32_e32 v66, v93, v66
	v_exp_f32_e32 v96, v97
	v_add_f32_e32 v66, v94, v66
	v_exp_f32_e32 v97, v68
	v_add_f32_e32 v66, v82, v66
	v_exp_f32_e32 v162, v69
	v_add_f32_e32 v66, v83, v66
	v_exp_f32_e32 v163, v70
	v_add_f32_e32 v66, v95, v66
	v_exp_f32_e32 v164, v71
	v_add_f32_e32 v66, v96, v66
	v_exp_f32_e32 v165, v72
	v_add_f32_e32 v66, v97, v66
	v_exp_f32_e32 v166, v73
	v_add_f32_e32 v66, v162, v66
	v_exp_f32_e32 v167, v74
	v_add_f32_e32 v66, v163, v66
	v_exp_f32_e32 v168, v75
	v_add_f32_e32 v66, v164, v66
	v_exp_f32_e32 v169, v76
	v_add_f32_e32 v66, v165, v66
	v_exp_f32_e32 v170, v77
	v_add_f32_e32 v66, v166, v66
	v_exp_f32_e32 v171, v78
	v_add_f32_e32 v66, v167, v66
	v_exp_f32_e32 v172, v79
	v_add_f32_e32 v66, v168, v66
	v_add_f32_e32 v66, v169, v66
	v_exp_f32_e32 v0, v0
	v_add_f32_e32 v66, v170, v66
	v_add_f32_e32 v66, v171, v66
	v_add_f32_e32 v66, v172, v66
	v_add_f32_e32 v66, v173, v66
	v_add_f32_e32 v191, v0, v66
	v_mov_b32_e32 v217, v191
	s_nop 1
	v_permlane32_swap_b32_e32 v191, v217
	v_cvt_pk_bf16_f32 v66, v67, v80
	v_cvt_pk_bf16_f32 v67, v81, v84
	v_cvt_pk_bf16_f32 v68, v85, v86
	v_cvt_pk_bf16_f32 v69, v87, v88
	v_cvt_pk_bf16_f32 v70, v89, v90
	v_cvt_pk_bf16_f32 v71, v91, v92
	v_cvt_pk_bf16_f32 v72, v93, v94
	v_cvt_pk_bf16_f32 v73, v82, v83
	v_cvt_pk_bf16_f32 v74, v95, v96
	v_cvt_pk_bf16_f32 v75, v97, v162
	v_cvt_pk_bf16_f32 v76, v163, v164
	v_cvt_pk_bf16_f32 v77, v165, v166
	v_cvt_pk_bf16_f32 v78, v167, v168
	v_cvt_pk_bf16_f32 v79, v169, v170
	v_cvt_pk_bf16_f32 v80, v171, v172
	v_cvt_pk_bf16_f32 v81, v173, v0
	s_nop 0
	v_permlane32_swap_b32_e32 v66, v68
	v_permlane32_swap_b32_e32 v67, v69
	v_permlane32_swap_b32_e32 v70, v72
	v_permlane32_swap_b32_e32 v71, v73
	v_permlane32_swap_b32_e32 v74, v76
	v_permlane32_swap_b32_e32 v75, v77
	v_permlane32_swap_b32_e32 v78, v80
	v_permlane32_swap_b32_e32 v79, v81
	s_waitcnt vmcnt(7)
	ds_write_b128 v209, v[130:133] offset:8192
	s_waitcnt vmcnt(6)
	ds_write_b128 v209, v[134:137] offset:10240
	s_waitcnt vmcnt(5)
	ds_write_b128 v209, v[138:141] offset:8448
	s_waitcnt vmcnt(4)
	ds_write_b128 v209, v[142:145] offset:10496
	s_waitcnt vmcnt(3)
	ds_write_b128 v209, v[146:149] offset:12288
	s_waitcnt vmcnt(2)
	ds_write_b128 v209, v[150:153] offset:14336
	s_waitcnt vmcnt(1)
	ds_write_b128 v209, v[154:157] offset:12544
	s_waitcnt vmcnt(0)
	ds_write_b128 v209, v[158:161] offset:14592
	s_waitcnt lgkmcnt(0)
; #define FA_SBAR() __builtin_amdgcn_sched_barrier(0)
; #define AA_LOADKC(tile_) do { _Pragma("unroll") for (int i_ = 0; i_ < 16; ++i_) { int tk = cls + ((base + (tile_) * 64 + 4 * i_ + vkey) << sh); tk = tk < 0 ? 0 : (tk > SEQ - 1 ? SEQ - 1 : tk); \
;                     kc[i_] = *(const v4u*)(Zbc + (unsigned)tk * (NA * 2) + (ZA_K + vch * 8) * 2); } } while (0)
; template <int PASS>
; __device__ __forceinline__ void attn_a_pass(LAS unsigned char* lds_all, const bf16* ZA, bf16* Oabc, float* ML, const float* rel_bias, int gw, int ngw, int xcd, int inx, int tid) {
;     ...
;                 { const int tn = (tile + 1 < ntile) ? tile + 1 : tile; AA_LOADKC(tn); }
;                 FA_SBAR();
;                 pv_d0(o, vb, pa0, pa1, pa2, pa3);
	s_add_i32 s6, s84, 1
	s_cmp_lt_u32 s6, s89
	s_cselect_b32 s7, s6, s84
	v_lshl_add_u32 v172, s7, 6, v210
	v_lshlrev_b32_e32 v0, s83, v172
	v_add_u32_e32 v0, s86, v0
	v_med3_i32 v0, v0, 0, v230
	v_mul_u32_u24_e32 v0, 0x1800, v0
	v_lshl_add_u64 v[82:83], v[192:193], 0, v[0:1]
	v_add_lshl_u32 v0, v172, 4, s83
	v_add_u32_e32 v0, s86, v0
	v_med3_i32 v0, v0, 0, v230
	v_mul_u32_u24_e32 v0, 0x1800, v0
	v_lshl_add_u64 v[86:87], v[192:193], 0, v[0:1]
	v_add_lshl_u32 v0, v172, 8, s83
	v_add_u32_e32 v0, s86, v0
	v_med3_i32 v0, v0, 0, v230
	v_mul_u32_u24_e32 v0, 0x1800, v0
	v_lshl_add_u64 v[90:91], v[192:193], 0, v[0:1]
	v_add_lshl_u32 v0, v172, 12, s83
	v_add_u32_e32 v0, s86, v0
	v_med3_i32 v0, v0, 0, v230
	v_mul_u32_u24_e32 v0, 0x1800, v0
	v_lshl_add_u64 v[94:95], v[192:193], 0, v[0:1]
	v_add_lshl_u32 v0, v172, 16, s83
	v_add_u32_e32 v0, s86, v0
	v_med3_i32 v0, v0, 0, v230
	v_mul_u32_u24_e32 v0, 0x1800, v0
	v_lshl_add_u64 v[130:131], v[192:193], 0, v[0:1]
	v_add_lshl_u32 v0, v172, 20, s83
	v_add_u32_e32 v0, s86, v0
	v_med3_i32 v0, v0, 0, v230
	v_mul_u32_u24_e32 v0, 0x1800, v0
	v_lshl_add_u64 v[134:135], v[192:193], 0, v[0:1]
	v_add_lshl_u32 v0, v172, 24, s83
	v_add_u32_e32 v0, s86, v0
	v_med3_i32 v0, v0, 0, v230
	v_mul_u32_u24_e32 v0, 0x1800, v0
	v_lshl_add_u64 v[138:139], v[192:193], 0, v[0:1]
	v_add_lshl_u32 v0, v172, 28, s83
	v_add_u32_e32 v0, s86, v0
	v_med3_i32 v0, v0, 0, v230
	v_mul_u32_u24_e32 v0, 0x1800, v0
	v_lshl_add_u64 v[142:143], v[192:193], 0, v[0:1]
	v_add_lshl_u32 v0, v172, 32, s83
	v_add_u32_e32 v0, s86, v0
	v_med3_i32 v0, v0, 0, v230
	v_mul_u32_u24_e32 v0, 0x1800, v0
	v_lshl_add_u64 v[146:147], v[192:193], 0, v[0:1]
	v_add_lshl_u32 v0, v172, 36, s83
	v_add_u32_e32 v0, s86, v0
	v_med3_i32 v0, v0, 0, v230
	v_mul_u32_u24_e32 v0, 0x1800, v0
	v_lshl_add_u64 v[150:151], v[192:193], 0, v[0:1]
	v_add_lshl_u32 v0, v172, 40, s83
	v_add_u32_e32 v0, s86, v0
	v_med3_i32 v0, v0, 0, v230
	v_mul_u32_u24_e32 v0, 0x1800, v0
	v_lshl_add_u64 v[154:155], v[192:193], 0, v[0:1]
	v_add_lshl_u32 v0, v172, 44, s83
	v_add_u32_e32 v0, s86, v0
	v_med3_i32 v0, v0, 0, v230
	v_mul_u32_u24_e32 v0, 0x1800, v0
	v_lshl_add_u64 v[158:159], v[192:193], 0, v[0:1]
	v_add_lshl_u32 v0, v172, 48, s83
	v_add_u32_e32 v0, s86, v0
	v_med3_i32 v0, v0, 0, v230
	v_mul_u32_u24_e32 v0, 0x1800, v0
	v_lshl_add_u64 v[162:163], v[192:193], 0, v[0:1]
	v_add_lshl_u32 v0, v172, 52, s83
	v_add_u32_e32 v0, s86, v0
	v_med3_i32 v0, v0, 0, v230
	v_mul_u32_u24_e32 v0, 0x1800, v0
	v_lshl_add_u64 v[166:167], v[192:193], 0, v[0:1]
	v_add_lshl_u32 v0, v172, 56, s83
	v_add_u32_e32 v0, s86, v0
	v_med3_i32 v0, v0, 0, v230
	v_mul_u32_u24_e32 v0, 0x1800, v0
	v_lshl_add_u64 v[170:171], v[192:193], 0, v[0:1]
	v_add_lshl_u32 v0, v172, 60, s83
	v_add_u32_e32 v0, s86, v0
	v_med3_i32 v0, v0, 0, v230
	v_mul_u32_u24_e32 v0, 0x1800, v0
	v_lshl_add_u64 v[174:175], v[192:193], 0, v[0:1]
	global_load_dwordx4 v[82:85], v[82:83], off offset:2048
	s_nop 0
	global_load_dwordx4 v[86:89], v[86:87], off offset:2048
	s_nop 0
	global_load_dwordx4 v[90:93], v[90:91], off offset:2048
	s_nop 0
	global_load_dwordx4 v[94:97], v[94:95], off offset:2048
	s_nop 0
	global_load_dwordx4 v[130:133], v[130:131], off offset:2048
	s_nop 0
	global_load_dwordx4 v[134:137], v[134:135], off offset:2048
	s_nop 0
	global_load_dwordx4 v[138:141], v[138:139], off offset:2048
	s_nop 0
	global_load_dwordx4 v[142:145], v[142:143], off offset:2048
	s_nop 0
	global_load_dwordx4 v[146:149], v[146:147], off offset:2048
	s_nop 0
	global_load_dwordx4 v[150:153], v[150:151], off offset:2048
	s_nop 0
	global_load_dwordx4 v[154:157], v[154:155], off offset:2048
	s_nop 0
	global_load_dwordx4 v[158:161], v[158:159], off offset:2048
	s_nop 0
	global_load_dwordx4 v[162:165], v[162:163], off offset:2048
	s_nop 0
	global_load_dwordx4 v[166:169], v[166:167], off offset:2048
	s_nop 0
	global_load_dwordx4 v[170:173], v[170:171], off offset:2048
	s_nop 0
	global_load_dwordx4 v[174:177], v[174:175], off offset:2048
	s_cmp_ge_u32 s6, s89
	ds_read_b64_tr_b16 v[236:237], v199 offset:0
	ds_read_b64_tr_b16 v[238:239], v199 offset:0x800
	ds_read_b64_tr_b16 v[240:241], v199 offset:0x1000
	ds_read_b64_tr_b16 v[242:243], v199 offset:0x1800
	ds_read_b64_tr_b16 v[244:245], v199 offset:0x2000
	ds_read_b64_tr_b16 v[246:247], v199 offset:0x2800
	ds_read_b64_tr_b16 v[248:249], v199 offset:0x3000
	ds_read_b64_tr_b16 v[250:251], v199 offset:0x3800
	s_nop 0
	s_waitcnt lgkmcnt(6)
; #define FA_SBAR() __builtin_amdgcn_sched_barrier(0)
; #define AA_WRITEKC() do { _Pragma("unroll") for (int i_ = 0; i_ < 16; ++i_) *(LAS v4u*)(Vl + i_ * 1024 + ((i_ & 1) ? (kst0 ^ 64) : kst0)) = kc[i_]; } while (0)
;   s16x4 l0 = tr_read<BASE + v_rd_off(D0, 0, 0)>(vb), h0 = tr_read<BASE + v_rd_off(D0, 0, 1)>(vb), l1 = tr_read<BASE + v_rd_off(D0, 1, 0)>(vb), h1 = tr_read<BASE + v_rd_off(D0, 1, 1)>(vb);
;   s16x4 l2 = tr_read<BASE + v_rd_off(D0, 2, 0)>(vb), h2 = tr_read<BASE + v_rd_off(D0, 2, 1)>(vb), l3 = tr_read<BASE + v_rd_off(D0, 3, 0)>(vb), h3 = tr_read<BASE + v_rd_off(D0, 3, 1)>(vb);
;   asm volatile("s_waitcnt lgkmcnt(0)" : "+v"(l0), "+v"(h0), "+v"(l1), "+v"(h1), "+v"(l2), "+v"(h2), "+v"(l3), "+v"(h3) :: "memory"); FA_SBAR();
;     ...
;   od = __builtin_amdgcn_mfma_f32_32x32x16_bf16(pa0, FA_PK(l0, h0), od, 0, 0, 0);
;   od = __builtin_amdgcn_mfma_f32_32x32x16_bf16(pa1, FA_PK(l1, h1), od, 0, 0, 0);
;   od = __builtin_amdgcn_mfma_f32_32x32x16_bf16(pa2, FA_PK(l2, h2), od, 0, 0, 0);
;   od = __builtin_amdgcn_mfma_f32_32x32x16_bf16(pa3, FA_PK(l3, h3), od, 0, 0, 0);
;     ...
; }
;   pv_one<0, BASE>(o[0], vb, pa0, pa1, pa2, pa3); pv_one<1, BASE>(o[1], vb, pa0, pa1, pa2, pa3); pv_one<2, BASE>(o[2], vb, pa0, pa1, pa2, pa3); pv_one<3, BASE>(o[3], vb, pa0, pa1, pa2, pa3);
; template <int PASS>
; __device__ __forceinline__ void attn_a_pass(LAS unsigned char* lds_all, const bf16* ZA, bf16* Oabc, float* ML, const float* rel_bias, int gw, int ngw, int xcd, int inx, int tid) {
;     ...
;                 if (tile + 1 < ntile) AA_WRITEKC();
	s_nop 0
	v_mfma_f32_32x32x16_bf16 v[50:65], v[66:69], v[236:239], v[50:65]
	ds_read_b64_tr_b16 v[236:237], v199 offset:0x200
	ds_read_b64_tr_b16 v[238:239], v199 offset:0xa00
	s_waitcnt lgkmcnt(6)
	v_mfma_f32_32x32x16_bf16 v[50:65], v[70:73], v[240:243], v[50:65]
	ds_read_b64_tr_b16 v[240:241], v199 offset:0x1200
	ds_read_b64_tr_b16 v[242:243], v199 offset:0x1a00
	s_waitcnt lgkmcnt(6)
	v_mfma_f32_32x32x16_bf16 v[50:65], v[74:77], v[244:247], v[50:65]
	ds_read_b64_tr_b16 v[244:245], v199 offset:0x2200
	ds_read_b64_tr_b16 v[246:247], v199 offset:0x2a00
	s_waitcnt lgkmcnt(6)
	v_mfma_f32_32x32x16_bf16 v[50:65], v[78:81], v[248:251], v[50:65]
	ds_read_b64_tr_b16 v[248:249], v199 offset:0x3200
	ds_read_b64_tr_b16 v[250:251], v199 offset:0x3a00
	s_nop 0
	s_waitcnt lgkmcnt(6)
	s_nop 0
	v_mfma_f32_32x32x16_bf16 v[34:49], v[66:69], v[236:239], v[34:49]
	ds_read_b64_tr_b16 v[236:237], v199 offset:0x400
	ds_read_b64_tr_b16 v[238:239], v199 offset:0xc00
	s_waitcnt lgkmcnt(6)
	v_mfma_f32_32x32x16_bf16 v[34:49], v[70:73], v[240:243], v[34:49]
	ds_read_b64_tr_b16 v[240:241], v199 offset:0x1400
	ds_read_b64_tr_b16 v[242:243], v199 offset:0x1c00
	s_waitcnt lgkmcnt(6)
	v_mfma_f32_32x32x16_bf16 v[34:49], v[74:77], v[244:247], v[34:49]
	ds_read_b64_tr_b16 v[244:245], v199 offset:0x2400
	ds_read_b64_tr_b16 v[246:247], v199 offset:0x2c00
	s_waitcnt lgkmcnt(6)
	v_mfma_f32_32x32x16_bf16 v[34:49], v[78:81], v[248:251], v[34:49]
	ds_read_b64_tr_b16 v[248:249], v199 offset:0x3400
	ds_read_b64_tr_b16 v[250:251], v199 offset:0x3c00
	s_nop 0
	s_waitcnt lgkmcnt(6)
	s_nop 0
	v_mfma_f32_32x32x16_bf16 v[18:33], v[66:69], v[236:239], v[18:33]
	ds_read_b64_tr_b16 v[236:237], v199 offset:0x600
	ds_read_b64_tr_b16 v[238:239], v199 offset:0xe00
	s_waitcnt lgkmcnt(6)
	v_mfma_f32_32x32x16_bf16 v[18:33], v[70:73], v[240:243], v[18:33]
	ds_read_b64_tr_b16 v[240:241], v199 offset:0x1600
	ds_read_b64_tr_b16 v[242:243], v199 offset:0x1e00
	s_waitcnt lgkmcnt(6)
	v_mfma_f32_32x32x16_bf16 v[18:33], v[74:77], v[244:247], v[18:33]
	ds_read_b64_tr_b16 v[244:245], v199 offset:0x2600
	ds_read_b64_tr_b16 v[246:247], v199 offset:0x2e00
	s_waitcnt lgkmcnt(6)
	v_mfma_f32_32x32x16_bf16 v[18:33], v[78:81], v[248:251], v[18:33]
	ds_read_b64_tr_b16 v[248:249], v199 offset:0x3600
	ds_read_b64_tr_b16 v[250:251], v199 offset:0x3e00
	s_nop 0
	s_waitcnt lgkmcnt(6)
	s_nop 0
	v_mfma_f32_32x32x16_bf16 v[2:17], v[66:69], v[236:239], v[2:17]
	s_waitcnt lgkmcnt(4)
	v_mfma_f32_32x32x16_bf16 v[2:17], v[70:73], v[240:243], v[2:17]
	s_waitcnt lgkmcnt(2)
	v_mfma_f32_32x32x16_bf16 v[2:17], v[74:77], v[244:247], v[2:17]
	s_waitcnt lgkmcnt(0)
	v_mfma_f32_32x32x16_bf16 v[2:17], v[78:81], v[248:251], v[2:17]
	s_cbranch_scc1 .LBB0_1030
	s_waitcnt vmcnt(15)
	ds_write_b128 v211, v[82:85]
	s_waitcnt vmcnt(14)
	ds_write_b128 v208, v[86:89] offset:1024
	s_waitcnt vmcnt(13)
	ds_write_b128 v211, v[90:93] offset:2048
	s_waitcnt vmcnt(12)
	ds_write_b128 v208, v[94:97] offset:3072
	s_waitcnt vmcnt(11)
	ds_write_b128 v211, v[130:133] offset:4096
	s_waitcnt vmcnt(10)
	ds_write_b128 v208, v[134:137] offset:5120
	s_waitcnt vmcnt(9)
	ds_write_b128 v211, v[138:141] offset:6144
	s_waitcnt vmcnt(8)
	ds_write_b128 v208, v[142:145] offset:7168
	s_waitcnt vmcnt(7)
	ds_write_b128 v211, v[146:149] offset:8192
	s_waitcnt vmcnt(6)
	ds_write_b128 v208, v[150:153] offset:9216
	s_waitcnt vmcnt(5)
	ds_write_b128 v211, v[154:157] offset:10240
	s_waitcnt vmcnt(4)
	ds_write_b128 v208, v[158:161] offset:11264
	s_waitcnt vmcnt(3)
	ds_write_b128 v211, v[162:165] offset:12288
	s_waitcnt vmcnt(2)
	ds_write_b128 v208, v[166:169] offset:13312
	s_waitcnt vmcnt(1)
	ds_write_b128 v211, v[170:173] offset:14336
	s_waitcnt vmcnt(0)
	ds_write_b128 v208, v[174:177] offset:15360
